# merge-phase K-loop: counted LDS-DMA wait moved from the top of the LOAD segment to just before its closing barrier (counts +3 for the stage issued in between)
# baseline (speedup 1.0000x reference)
.LBB0_2056:
	s_mul_i32 s26, s34, 0x6000
	s_add_i32 s26, s26, 0
	s_add_i32 s27, s26, s36
	v_add_u32_e32 v2, s27, v133
	s_add_i32 s26, s26, s37
	ds_read_b128 v[142:145], v2
	ds_read_b128 v[146:149], v2 offset:1024
	ds_read_b128 v[150:153], v2 offset:2048
	ds_read_b128 v[154:157], v2 offset:3072
	v_add_u32_e32 v2, s26, v133
	ds_read_b128 v[158:161], v2 offset:16384
	ds_read_b128 v[162:165], v2 offset:17408
	ds_read_b128 v[166:169], v2 offset:18432
	ds_read_b128 v[170:173], v2 offset:19456
	s_cmp_gt_u32 s28, 10
	s_cbranch_scc1 .Lmy_mw_done
	s_cmp_lt_u32 s28, 2
	s_cselect_b64 s[26:27], -1, 0
	s_and_b64 s[26:27], s[16:17], s[26:27]
	s_and_b64 vcc, exec, s[26:27]
	s_cbranch_vccz .Lmy_mw_b
	s_waitcnt vmcnt(10)
	s_branch .Lmy_mw_done
.Lmy_mw_b:
	s_cmp_lt_u32 s28, 9
	s_cselect_b64 s[26:27], -1, 0
	s_or_b64 s[26:27], s[18:19], s[26:27]
	s_and_b64 vcc, exec, s[26:27]
	s_cbranch_vccz .Lmy_mw_c
	s_waitcnt vmcnt(6)
	s_branch .Lmy_mw_done
.Lmy_mw_c:
	s_cmp_eq_u32 s28, 9
	s_cbranch_scc0 .Lmy_mw_d
	s_waitcnt vmcnt(3)
	s_branch .Lmy_mw_done

.Lmy_mw_done:
	s_barrier
	s_add_i32 s28, s28, 1
	s_setprio 1
	s_waitcnt lgkmcnt(3)
	v_mfma_f32_16x16x32_bf16 v[64:67], v[158:161], v[142:145], v[64:67]
	s_waitcnt lgkmcnt(2)
	v_mfma_f32_16x16x32_bf16 v[60:63], v[162:165], v[142:145], v[60:63]
	s_waitcnt lgkmcnt(1)
	v_mfma_f32_16x16x32_bf16 v[56:59], v[166:169], v[142:145], v[56:59]
	s_waitcnt lgkmcnt(0)
	v_mfma_f32_16x16x32_bf16 v[52:55], v[170:173], v[142:145], v[52:55]
	v_mfma_f32_16x16x32_bf16 v[48:51], v[158:161], v[146:149], v[48:51]
	v_mfma_f32_16x16x32_bf16 v[44:47], v[162:165], v[146:149], v[44:47]
	v_mfma_f32_16x16x32_bf16 v[40:43], v[166:169], v[146:149], v[40:43]
	v_mfma_f32_16x16x32_bf16 v[36:39], v[170:173], v[146:149], v[36:39]
	v_mfma_f32_16x16x32_bf16 v[32:35], v[158:161], v[150:153], v[32:35]
	v_mfma_f32_16x16x32_bf16 v[28:31], v[162:165], v[150:153], v[28:31]
	v_mfma_f32_16x16x32_bf16 v[24:27], v[166:169], v[150:153], v[24:27]
	v_mfma_f32_16x16x32_bf16 v[20:23], v[170:173], v[150:153], v[20:23]
	v_mfma_f32_16x16x32_bf16 v[16:19], v[158:161], v[154:157], v[16:19]
	v_mfma_f32_16x16x32_bf16 v[12:15], v[162:165], v[154:157], v[12:15]
	v_mfma_f32_16x16x32_bf16 v[8:11], v[166:169], v[154:157], v[8:11]
	v_mfma_f32_16x16x32_bf16 v[4:7], v[170:173], v[154:157], v[4:7]
	s_setprio 0
	s_add_i32 s26, s34, 1
	s_cmp_lg_u32 s34, 4
	s_cselect_b32 s34, s26, 0
	s_add_i32 s26, s59, 1
	s_cmp_lg_u32 s59, 4
	s_cselect_b32 s59, s26, 0
	s_add_i32 s50, s50, 32
	s_add_u32 s20, s20, 64
	s_addc_u32 s21, s21, 0
	s_barrier
	s_add_u32 s22, s22, 64
	s_addc_u32 s23, s23, 0
	s_cmp_eq_u32 s28, 12
	s_cbranch_scc1 .LBB0_2072
.LBB0_2057:
.LBB0_2066:
	s_cmp_gt_u32 s28, 8
	s_mov_b64 s[26:27], -1
	s_cbranch_scc0 .LBB0_2070
	s_andn2_b64 vcc, exec, s[18:19]
	s_cbranch_vccnz .LBB0_2069
	s_mul_i32 s26, s59, 0x6000
	s_add_i32 s64, s26, 0
	s_lshl_b64 s[26:27], s[50:51], 1
	s_add_u32 s62, s29, s26
	s_addc_u32 s63, s30, s27
	s_add_u32 s26, s31, s26
	s_addc_u32 s27, s58, s27
	s_add_i32 s64, s35, s64
	s_mov_b32 s65, m0
	s_mov_b32 m0, s64
	s_nop 0
	global_load_lds_dwordx4 v134, s[62:63]
	s_mov_b32 m0, s65
	s_add_i32 s65, s64, 0x2000
	s_mov_b32 s66, m0
	s_mov_b32 m0, s65
	s_nop 0
	global_load_lds_dwordx4 v135, s[62:63]
	s_mov_b32 m0, s66
	s_addk_i32 s64, 0x4000
	s_mov_b32 s62, m0
	s_mov_b32 m0, s64
	s_nop 0
	global_load_lds_dwordx4 v136, s[26:27]
	s_mov_b32 m0, s62
